# P2 S^T LDS fragment reads hoisted with register-ring renaming only (no chunk prefetch)
# baseline (speedup 1.0000x reference)
.LBB0_260:
	v_lshl_add_u64 v[4:5], v[96:97], 0, s[20:21]
	v_add_co_u32_e32 v22, vcc, s65, v4
	s_nop 1
	v_addc_co_u32_e32 v23, vcc, 0, v5, vcc
	v_add_co_u32_e32 v24, vcc, s66, v4
	s_nop 1
	v_addc_co_u32_e32 v25, vcc, 0, v5, vcc
	global_load_dwordx4 v[54:57], v[22:23], off
	global_load_dwordx4 v[58:61], v[24:25], off
	v_add_co_u32_e32 v22, vcc, s67, v4
	s_nop 1
	v_addc_co_u32_e32 v23, vcc, 0, v5, vcc
	v_add_co_u32_e32 v24, vcc, s68, v4
	s_nop 1
	v_addc_co_u32_e32 v25, vcc, 0, v5, vcc
	global_load_dwordx4 v[62:65], v[22:23], off
	global_load_dwordx4 v[66:69], v[24:25], off
	v_add_co_u32_e32 v22, vcc, s69, v4
	s_nop 1
	v_addc_co_u32_e32 v23, vcc, 0, v5, vcc
	v_add_co_u32_e32 v24, vcc, s70, v4
	s_nop 1
	v_addc_co_u32_e32 v25, vcc, 0, v5, vcc
	global_load_dwordx4 v[70:73], v[22:23], off
	global_load_dwordx4 v[174:177], v[24:25], off
	v_add_co_u32_e32 v22, vcc, s71, v4
	s_nop 1
	v_addc_co_u32_e32 v23, vcc, 0, v5, vcc
	v_add_co_u32_e32 v4, vcc, s72, v4
	s_nop 1
	v_addc_co_u32_e32 v5, vcc, 0, v5, vcc
	global_load_dwordx4 v[178:181], v[22:23], off
	global_load_dwordx4 v[182:185], v[4:5], off
	v_lshl_add_u64 v[4:5], v[94:95], 0, s[20:21]
	v_add_co_u32_e32 v22, vcc, s73, v4
	s_nop 1
	v_addc_co_u32_e32 v23, vcc, 0, v5, vcc
	global_load_dwordx2 v[186:187], v[22:23], off
	v_add_co_u32_e32 v4, vcc, s75, v4
	s_nop 1
	v_addc_co_u32_e32 v5, vcc, 0, v5, vcc
	global_load_dwordx2 v[4:5], v[4:5], off
	v_lshl_add_u64 v[22:23], v[98:99], 0, s[20:21]
	global_load_dwordx4 v[50:53], v[22:23], off offset:-256
	global_load_dwordx4 v[46:49], v[22:23], off offset:-192
	global_load_dwordx4 v[42:45], v[22:23], off offset:-128
	global_load_dwordx4 v[38:41], v[22:23], off offset:-64
	global_load_dwordx4 v[34:37], v[22:23], off
	global_load_dwordx4 v[30:33], v[22:23], off offset:64
	global_load_dwordx4 v[26:29], v[22:23], off offset:128
	s_nop 0
	global_load_dwordx4 v[22:25], v[22:23], off offset:192
	s_andn2_b64 vcc, exec, s[26:27]
	s_waitcnt vmcnt(17)
	ds_write_b128 v116, v[54:57]
	s_waitcnt vmcnt(16)
	ds_write_b128 v116, v[58:61] offset:4096
	s_waitcnt vmcnt(15)
	ds_write_b128 v116, v[62:65] offset:8192
	s_waitcnt vmcnt(14)
	ds_write_b128 v116, v[66:69] offset:12288
	s_waitcnt vmcnt(13)
	ds_write_b128 v116, v[70:73] offset:16384
	s_waitcnt vmcnt(12)
	ds_write_b128 v116, v[174:177] offset:20480
	s_waitcnt vmcnt(11)
	ds_write_b128 v116, v[178:181] offset:24576
	s_waitcnt vmcnt(10)
	ds_write_b128 v116, v[182:185] offset:28672
	s_waitcnt vmcnt(9)
	ds_write_b16 v101, v186
	ds_write_b16_d16_hi v101, v186 offset:272
	ds_write_b16 v101, v187 offset:544
	ds_write_b16_d16_hi v101, v187 offset:816
	v_lshlrev_b32_e32 v3, 16, v186
	v_and_b32_e32 v54, 0xffff0000, v186
	v_lshlrev_b32_e32 v55, 16, v187
	v_mul_f32_e32 v3, v172, v3
	v_mul_f32_e32 v54, v172, v54
	v_mul_f32_e32 v55, v172, v55
	v_bfe_u32 v56, v3, 16, 1
	v_bfe_u32 v57, v54, 16, 1
	v_bfe_u32 v58, v55, 16, 1
	v_add3_u32 v3, v3, v56, s74
	v_add3_u32 v54, v54, v57, s74
	v_add3_u32 v55, v55, v58, s74
	ds_write_b16_d16_hi v102, v3
	ds_write_b16_d16_hi v102, v54 offset:272
	ds_write_b16_d16_hi v102, v55 offset:544
	v_and_b32_e32 v3, 0xffff0000, v187
	v_mul_f32_e32 v3, v172, v3
	v_bfe_u32 v54, v3, 16, 1
	v_add3_u32 v3, v3, v54, s74
	ds_write_b16_d16_hi v102, v3 offset:816
	s_waitcnt vmcnt(8)
	ds_write_b16 v101, v4 offset:128
	ds_write_b16_d16_hi v101, v4 offset:400
	ds_write_b16 v101, v5 offset:672
	ds_write_b16_d16_hi v101, v5 offset:944
	v_lshlrev_b32_e32 v3, 16, v4
	v_mul_f32_e32 v3, v173, v3
	v_bfe_u32 v54, v3, 16, 1
	v_add3_u32 v3, v3, v54, s74
	ds_write_b16_d16_hi v102, v3 offset:128
	v_and_b32_e32 v3, 0xffff0000, v4
	v_mul_f32_e32 v3, v173, v3
	v_bfe_u32 v4, v3, 16, 1
	v_add3_u32 v3, v3, v4, s74
	ds_write_b16_d16_hi v102, v3 offset:400
	v_lshlrev_b32_e32 v3, 16, v5
	v_mul_f32_e32 v3, v173, v3
	v_bfe_u32 v4, v3, 16, 1
	v_add3_u32 v3, v3, v4, s74
	ds_write_b16_d16_hi v102, v3 offset:672
	v_and_b32_e32 v3, 0xffff0000, v5
	v_mul_f32_e32 v3, v173, v3
	v_bfe_u32 v4, v3, 16, 1
	v_add3_u32 v3, v3, v4, s74
	ds_write_b16_d16_hi v102, v3 offset:944
	v_cndmask_b32_e64 v3, 0, 1, s[26:27]
	v_cmp_ne_u32_e64 s[12:13], 1, v3
	v_mov_b32_e32 v57, 0
	v_mov_b32_e32 v56, 0
	v_mov_b32_e32 v55, 0
	v_mov_b32_e32 v54, 0
	s_waitcnt lgkmcnt(0)
	s_barrier
	s_cbranch_vccnz .LBB0_267
	ds_read_b128 v[62:65], v154
	ds_read_b128 v[66:69], v154 offset:4096
	ds_read_b128 v[70:73], v155
	ds_read_b128 v[174:177], v155 offset:4096
	ds_read_b128 v[178:181], v156
	ds_read_b128 v[182:185], v156 offset:4096
	ds_read_b128 v[186:189], v157
	ds_read_b128 v[190:193], v157 offset:4096
	s_andn2_b64 vcc, exec, s[2:3]
	s_waitcnt vmcnt(7)
	s_waitcnt lgkmcnt(7)
	v_mfma_f32_16x16x32_bf16 v[54:57], v[62:65], v[50:53], 0
	ds_read_b128 v[62:65], v154 offset:32768
	s_nop 0
	s_waitcnt lgkmcnt(7)
	v_mfma_f32_16x16x32_bf16 v[58:61], v[66:69], v[50:53], 0
	ds_read_b128 v[66:69], v154 offset:36864
	s_waitcnt vmcnt(6)
	s_waitcnt lgkmcnt(7)
	v_mfma_f32_16x16x32_bf16 v[54:57], v[70:73], v[46:49], v[54:57]
	ds_read_b128 v[70:73], v155 offset:32768
	s_nop 0
	s_waitcnt lgkmcnt(7)
	v_mfma_f32_16x16x32_bf16 v[58:61], v[174:177], v[46:49], v[58:61]
	ds_read_b128 v[174:177], v155 offset:36864
	s_waitcnt vmcnt(5)
	s_waitcnt lgkmcnt(7)
	v_mfma_f32_16x16x32_bf16 v[54:57], v[178:181], v[42:45], v[54:57]
	ds_read_b128 v[178:181], v156 offset:32768
	s_nop 0
	s_waitcnt lgkmcnt(7)
	v_mfma_f32_16x16x32_bf16 v[58:61], v[182:185], v[42:45], v[58:61]
	ds_read_b128 v[182:185], v156 offset:36864
	s_waitcnt vmcnt(4)
	s_waitcnt lgkmcnt(7)
	v_mfma_f32_16x16x32_bf16 v[54:57], v[186:189], v[38:41], v[54:57]
	ds_read_b128 v[186:189], v157 offset:32768
	s_nop 0
	s_waitcnt lgkmcnt(7)
	v_mfma_f32_16x16x32_bf16 v[58:61], v[190:193], v[38:41], v[58:61]
	ds_read_b128 v[190:193], v157 offset:36864
	s_waitcnt vmcnt(3)
	s_waitcnt lgkmcnt(7)
	v_mfma_f32_16x16x32_bf16 v[54:57], v[62:65], v[34:37], v[54:57]
	s_waitcnt vmcnt(2)
	s_waitcnt lgkmcnt(5)
	v_mfma_f32_16x16x32_bf16 v[54:57], v[70:73], v[30:33], v[54:57]
	s_waitcnt vmcnt(1)
	s_waitcnt lgkmcnt(3)
	v_mfma_f32_16x16x32_bf16 v[54:57], v[178:181], v[26:29], v[54:57]
	v_mfma_f32_16x16x32_bf16 v[58:61], v[66:69], v[34:37], v[58:61]
	s_waitcnt vmcnt(0)
	s_waitcnt lgkmcnt(1)
	v_mfma_f32_16x16x32_bf16 v[54:57], v[186:189], v[22:25], v[54:57]
	v_mfma_f32_16x16x32_bf16 v[58:61], v[174:177], v[30:33], v[58:61]
	s_nop 6
	v_mul_f32_e32 v3, v54, v160
	v_mul_f32_e32 v5, v56, v160
	v_mul_f32_e32 v54, v57, v160
	v_mfma_f32_16x16x32_bf16 v[56:59], v[182:185], v[26:29], v[58:61]
	v_mul_f32_e32 v4, v55, v160
	v_mul_f32_e32 v3, v3, v168
	v_mul_f32_e32 v4, v4, v169
	s_nop 0
	s_waitcnt lgkmcnt(0)
	v_mfma_f32_16x16x32_bf16 v[58:61], v[190:193], v[22:25], v[56:59]
	v_mul_f32_e32 v5, v5, v170
	v_mul_f32_e32 v55, v54, v171
	s_cbranch_vccnz .LBB0_263
	v_cndmask_b32_e64 v3, 0, v3, s[4:5]
	v_cndmask_b32_e64 v4, 0, v4, s[6:7]
	v_cndmask_b32_e64 v5, 0, v5, s[8:9]
	v_cndmask_b32_e64 v55, 0, v55, s[10:11]

.LBB0_267:
	v_cndmask_b32_e64 v3, 0, 1, s[30:31]
	v_mov_b32_e32 v61, 0
	v_cmp_ne_u32_e64 s[14:15], 1, v3
	s_andn2_b64 vcc, exec, s[30:31]
	v_mov_b32_e32 v60, 0
	v_mov_b32_e32 v59, 0
	v_mov_b32_e32 v58, 0
	s_cbranch_vccnz .LBB0_274
	ds_read_b128 v[66:69], v154 offset:8192
	ds_read_b128 v[70:73], v154 offset:12288
	ds_read_b128 v[174:177], v155 offset:8192
	ds_read_b128 v[178:181], v155 offset:12288
	ds_read_b128 v[182:185], v156 offset:8192
	ds_read_b128 v[186:189], v156 offset:12288
	ds_read_b128 v[190:193], v157 offset:8192
	s_andn2_b64 vcc, exec, s[34:35]
	s_waitcnt vmcnt(7)
	s_waitcnt lgkmcnt(6)
	v_mfma_f32_16x16x32_bf16 v[58:61], v[66:69], v[50:53], 0
	ds_read_b128 v[66:69], v157 offset:12288
	s_nop 0
	s_waitcnt lgkmcnt(6)
	v_mfma_f32_16x16x32_bf16 v[62:65], v[70:73], v[50:53], 0
	ds_read_b128 v[70:73], v154 offset:40960
	s_waitcnt vmcnt(6)
	s_waitcnt lgkmcnt(6)
	v_mfma_f32_16x16x32_bf16 v[58:61], v[174:177], v[46:49], v[58:61]
	ds_read_b128 v[174:177], v154 offset:45056
	s_nop 0
	s_waitcnt lgkmcnt(6)
	v_mfma_f32_16x16x32_bf16 v[62:65], v[178:181], v[46:49], v[62:65]
	ds_read_b128 v[178:181], v155 offset:40960
	s_waitcnt vmcnt(5)
	s_waitcnt lgkmcnt(6)
	v_mfma_f32_16x16x32_bf16 v[58:61], v[182:185], v[42:45], v[58:61]
	ds_read_b128 v[182:185], v155 offset:45056
	s_nop 0
	s_waitcnt lgkmcnt(6)
	v_mfma_f32_16x16x32_bf16 v[62:65], v[186:189], v[42:45], v[62:65]
	ds_read_b128 v[186:189], v156 offset:40960
	s_waitcnt vmcnt(4)
	s_waitcnt lgkmcnt(6)
	v_mfma_f32_16x16x32_bf16 v[58:61], v[190:193], v[38:41], v[58:61]
	ds_read_b128 v[190:193], v156 offset:45056
	s_nop 0
	s_waitcnt lgkmcnt(6)
	v_mfma_f32_16x16x32_bf16 v[62:65], v[66:69], v[38:41], v[62:65]
	ds_read_b128 v[66:69], v157 offset:40960
	s_waitcnt vmcnt(3)
	s_waitcnt lgkmcnt(6)
	v_mfma_f32_16x16x32_bf16 v[58:61], v[70:73], v[34:37], v[58:61]
	ds_read_b128 v[70:73], v157 offset:45056
	s_waitcnt vmcnt(2)
	s_waitcnt lgkmcnt(5)
	v_mfma_f32_16x16x32_bf16 v[58:61], v[178:181], v[30:33], v[58:61]
	s_waitcnt vmcnt(1)
	s_waitcnt lgkmcnt(3)
	v_mfma_f32_16x16x32_bf16 v[58:61], v[186:189], v[26:29], v[58:61]
	v_mfma_f32_16x16x32_bf16 v[62:65], v[174:177], v[34:37], v[62:65]
	s_waitcnt vmcnt(0)
	s_waitcnt lgkmcnt(1)
	v_mfma_f32_16x16x32_bf16 v[58:61], v[66:69], v[22:25], v[58:61]
	v_mfma_f32_16x16x32_bf16 v[62:65], v[182:185], v[30:33], v[62:65]
	s_nop 6
	v_mul_f32_e32 v3, v58, v162
	v_mul_f32_e32 v5, v60, v162
	v_mul_f32_e32 v58, v61, v162
	v_mfma_f32_16x16x32_bf16 v[60:63], v[190:193], v[26:29], v[62:65]
	v_mul_f32_e32 v4, v59, v162
	v_mul_f32_e32 v3, v3, v168
	v_mul_f32_e32 v4, v4, v169
	s_nop 0
	s_waitcnt lgkmcnt(0)
	v_mfma_f32_16x16x32_bf16 v[62:65], v[70:73], v[22:25], v[60:63]
	v_mul_f32_e32 v5, v5, v170
	v_mul_f32_e32 v59, v58, v171
	s_cbranch_vccnz .LBB0_270
	v_cndmask_b32_e64 v3, 0, v3, s[4:5]
	v_cndmask_b32_e64 v4, 0, v4, s[6:7]
	v_cndmask_b32_e64 v5, 0, v5, s[8:9]
	v_cndmask_b32_e64 v59, 0, v59, s[10:11]

.LBB0_274:
	v_cndmask_b32_e64 v3, 0, 1, s[40:41]
	v_mov_b32_e32 v65, 0
	v_cmp_ne_u32_e64 s[16:17], 1, v3
	s_andn2_b64 vcc, exec, s[40:41]
	v_mov_b32_e32 v64, 0
	v_mov_b32_e32 v63, 0
	v_mov_b32_e32 v62, 0
	s_cbranch_vccnz .LBB0_281
	ds_read_b128 v[70:73], v154 offset:16384
	ds_read_b128 v[174:177], v154 offset:20480
	ds_read_b128 v[178:181], v155 offset:16384
	ds_read_b128 v[182:185], v155 offset:20480
	ds_read_b128 v[186:189], v156 offset:16384
	ds_read_b128 v[190:193], v156 offset:20480
	s_andn2_b64 vcc, exec, s[42:43]
	s_waitcnt vmcnt(7)
	s_waitcnt lgkmcnt(5)
	v_mfma_f32_16x16x32_bf16 v[62:65], v[70:73], v[50:53], 0
	ds_read_b128 v[70:73], v157 offset:16384
	s_nop 0
	s_waitcnt lgkmcnt(5)
	v_mfma_f32_16x16x32_bf16 v[66:69], v[174:177], v[50:53], 0
	ds_read_b128 v[174:177], v157 offset:20480
	s_waitcnt vmcnt(6)
	s_waitcnt lgkmcnt(5)
	v_mfma_f32_16x16x32_bf16 v[62:65], v[178:181], v[46:49], v[62:65]
	ds_read_b128 v[178:181], v154 offset:49152
	s_nop 0
	s_waitcnt lgkmcnt(5)
	v_mfma_f32_16x16x32_bf16 v[66:69], v[182:185], v[46:49], v[66:69]
	ds_read_b128 v[182:185], v154 offset:53248
	s_waitcnt vmcnt(5)
	s_waitcnt lgkmcnt(5)
	v_mfma_f32_16x16x32_bf16 v[62:65], v[186:189], v[42:45], v[62:65]
	ds_read_b128 v[186:189], v155 offset:49152
	s_nop 0
	s_waitcnt lgkmcnt(5)
	v_mfma_f32_16x16x32_bf16 v[66:69], v[190:193], v[42:45], v[66:69]
	ds_read_b128 v[190:193], v155 offset:53248
	s_waitcnt vmcnt(4)
	s_waitcnt lgkmcnt(5)
	v_mfma_f32_16x16x32_bf16 v[62:65], v[70:73], v[38:41], v[62:65]
	ds_read_b128 v[70:73], v156 offset:49152
	s_nop 0
	s_waitcnt lgkmcnt(5)
	v_mfma_f32_16x16x32_bf16 v[66:69], v[174:177], v[38:41], v[66:69]
	ds_read_b128 v[174:177], v156 offset:53248
	s_waitcnt vmcnt(3)
	s_waitcnt lgkmcnt(5)
	v_mfma_f32_16x16x32_bf16 v[62:65], v[178:181], v[34:37], v[62:65]
	ds_read_b128 v[178:181], v157 offset:49152
	s_waitcnt vmcnt(2)
	s_waitcnt lgkmcnt(4)
	v_mfma_f32_16x16x32_bf16 v[62:65], v[186:189], v[30:33], v[62:65]
	ds_read_b128 v[186:189], v157 offset:53248
	s_waitcnt vmcnt(1)
	s_waitcnt lgkmcnt(3)
	v_mfma_f32_16x16x32_bf16 v[62:65], v[70:73], v[26:29], v[62:65]
	v_mfma_f32_16x16x32_bf16 v[66:69], v[182:185], v[34:37], v[66:69]
	s_waitcnt vmcnt(0)
	s_waitcnt lgkmcnt(1)
	v_mfma_f32_16x16x32_bf16 v[62:65], v[178:181], v[22:25], v[62:65]
	v_mfma_f32_16x16x32_bf16 v[66:69], v[190:193], v[30:33], v[66:69]
	s_nop 6
	v_mul_f32_e32 v3, v62, v164
	v_mul_f32_e32 v5, v64, v164
	v_mul_f32_e32 v62, v65, v164
	v_mfma_f32_16x16x32_bf16 v[64:67], v[174:177], v[26:29], v[66:69]
	v_mul_f32_e32 v4, v63, v164
	v_mul_f32_e32 v3, v3, v168
	v_mul_f32_e32 v4, v4, v169
	s_nop 0
	s_waitcnt lgkmcnt(0)
	v_mfma_f32_16x16x32_bf16 v[66:69], v[186:189], v[22:25], v[64:67]
	v_mul_f32_e32 v5, v5, v170
	v_mul_f32_e32 v63, v62, v171
	s_cbranch_vccnz .LBB0_277
	v_cndmask_b32_e64 v3, 0, v3, s[4:5]
	v_cndmask_b32_e64 v4, 0, v4, s[6:7]
	v_cndmask_b32_e64 v5, 0, v5, s[8:9]
	v_cndmask_b32_e64 v63, 0, v63, s[10:11]

.LBB0_281:
	v_cndmask_b32_e64 v3, 0, 1, s[48:49]
	v_mov_b32_e32 v69, 0
	v_cmp_ne_u32_e64 s[18:19], 1, v3
	s_andn2_b64 vcc, exec, s[48:49]
	v_mov_b32_e32 v68, 0
	v_mov_b32_e32 v67, 0
	v_mov_b32_e32 v66, 0
	s_cbranch_vccnz .LBB0_288
	ds_read_b128 v[174:177], v154 offset:24576
	ds_read_b128 v[178:181], v154 offset:28672
	ds_read_b128 v[182:185], v155 offset:24576
	ds_read_b128 v[186:189], v155 offset:28672
	ds_read_b128 v[190:193], v156 offset:24576
	s_andn2_b64 vcc, exec, s[50:51]
	s_waitcnt vmcnt(7)
	s_waitcnt lgkmcnt(4)
	v_mfma_f32_16x16x32_bf16 v[66:69], v[174:177], v[50:53], 0
	ds_read_b128 v[174:177], v156 offset:28672
	s_nop 0
	s_waitcnt lgkmcnt(4)
	v_mfma_f32_16x16x32_bf16 v[70:73], v[178:181], v[50:53], 0
	ds_read_b128 v[178:181], v157 offset:24576
	s_waitcnt vmcnt(6)
	s_waitcnt lgkmcnt(4)
	v_mfma_f32_16x16x32_bf16 v[66:69], v[182:185], v[46:49], v[66:69]
	ds_read_b128 v[182:185], v157 offset:28672
	s_nop 0
	s_waitcnt lgkmcnt(4)
	v_mfma_f32_16x16x32_bf16 v[70:73], v[186:189], v[46:49], v[70:73]
	ds_read_b128 v[186:189], v154 offset:57344
	s_waitcnt vmcnt(5)
	s_waitcnt lgkmcnt(4)
	v_mfma_f32_16x16x32_bf16 v[66:69], v[190:193], v[42:45], v[66:69]
	ds_read_b128 v[190:193], v154 offset:61440
	s_nop 0
	s_waitcnt lgkmcnt(4)
	v_mfma_f32_16x16x32_bf16 v[70:73], v[174:177], v[42:45], v[70:73]
	ds_read_b128 v[174:177], v155 offset:57344
	s_waitcnt vmcnt(4)
	s_waitcnt lgkmcnt(4)
	v_mfma_f32_16x16x32_bf16 v[66:69], v[178:181], v[38:41], v[66:69]
	ds_read_b128 v[178:181], v155 offset:61440
	s_nop 0
	s_waitcnt lgkmcnt(4)
	v_mfma_f32_16x16x32_bf16 v[70:73], v[182:185], v[38:41], v[70:73]
	ds_read_b128 v[182:185], v156 offset:57344
	s_waitcnt vmcnt(3)
	s_waitcnt lgkmcnt(4)
	v_mfma_f32_16x16x32_bf16 v[66:69], v[186:189], v[34:37], v[66:69]
	ds_read_b128 v[186:189], v156 offset:61440
	s_waitcnt vmcnt(2)
	s_waitcnt lgkmcnt(3)
	v_mfma_f32_16x16x32_bf16 v[66:69], v[174:177], v[30:33], v[66:69]
	ds_read_b128 v[174:177], v157 offset:57344
	s_waitcnt vmcnt(1)
	s_waitcnt lgkmcnt(2)
	v_mfma_f32_16x16x32_bf16 v[66:69], v[182:185], v[26:29], v[66:69]
	ds_read_b128 v[182:185], v157 offset:61440
	v_mfma_f32_16x16x32_bf16 v[70:73], v[190:193], v[34:37], v[70:73]
	s_waitcnt vmcnt(0)
	s_waitcnt lgkmcnt(1)
	v_mfma_f32_16x16x32_bf16 v[66:69], v[174:177], v[22:25], v[66:69]
	v_mfma_f32_16x16x32_bf16 v[70:73], v[178:181], v[30:33], v[70:73]
	s_nop 6
	v_mul_f32_e32 v3, v66, v166
	v_mul_f32_e32 v5, v68, v166
	v_mul_f32_e32 v66, v69, v166
	v_mfma_f32_16x16x32_bf16 v[68:71], v[186:189], v[26:29], v[70:73]
	v_mul_f32_e32 v4, v67, v166
	v_mul_f32_e32 v3, v3, v168
	v_mul_f32_e32 v4, v4, v169
	s_nop 0
	s_waitcnt lgkmcnt(0)
	v_mfma_f32_16x16x32_bf16 v[70:73], v[182:185], v[22:25], v[68:71]
	v_mul_f32_e32 v5, v5, v170
	v_mul_f32_e32 v67, v66, v171
	s_cbranch_vccnz .LBB0_284
	v_cndmask_b32_e64 v3, 0, v3, s[4:5]
	v_cndmask_b32_e64 v4, 0, v4, s[6:7]
	v_cndmask_b32_e64 v5, 0, v5, s[8:9]
	v_cndmask_b32_e64 v67, 0, v67, s[10:11]
